# tail converter f32 weight loads temporal (nt dropped) on top of hand-written P3 epilogue + write-back stores
# baseline (speedup 1.0000x reference)
; __device__ __forceinline__ void conv_load(const ConvItem& ci, int lane, float (&v)[64]) {
;     const bool okc = ci.srcc >= 0 && (ci.srcc + lane) < ci.ncols;
;     const float* base = ci.W + (okc ? ci.srcc + lane : 0);
;     const int kmax = ci.Ksrc - 1;
; #pragma unroll
;     for (int i = 0; i < 64; ++i) { const int k = ci.k0 + i, kk = k < kmax ? k : kmax; v[i] = __builtin_nontemporal_load(base + (size_t)kk * ci.ldw); }
.Lcvp10_90:
	v_cmp_lt_i32_e32 vcc, -1, v0
	v_add_u32_e32 v0, v0, v11
	v_cmp_gt_i32_e64 s[4:5], s77, v0
	s_and_b64 vcc, vcc, s[4:5]
	s_add_i32 s4, s76, -1
	v_ashrrev_i32_e32 v1, 31, v0
	s_min_i32 s5, s58, s4
	v_cndmask_b32_e32 v1, 0, v1, vcc
	v_cndmask_b32_e32 v0, 0, v0, vcc
	s_ashr_i32 s6, s5, 31
	v_lshl_add_u64 v[0:1], v[0:1], 2, s[64:65]
	s_mul_i32 s6, s6, s77
	s_mul_hi_u32 s7, s5, s77
	s_add_i32 s64, s58, 1
	s_add_i32 s7, s7, s6
	s_mul_i32 s6, s5, s77
	s_min_i32 s5, s64, s4
	v_lshl_add_u64 v[2:3], s[6:7], 2, v[0:1]
	s_ashr_i32 s6, s5, 31
	s_mul_i32 s6, s6, s77
	s_mul_hi_u32 s7, s5, s77
	s_add_i32 s65, s58, 2
	s_add_i32 s7, s7, s6
	s_mul_i32 s6, s5, s77
	s_min_i32 s5, s65, s4
	s_waitcnt vmcnt(0)
	v_lshl_add_u64 v[4:5], s[6:7], 2, v[0:1]
	s_ashr_i32 s6, s5, 31
	s_mul_i32 s6, s6, s77
	s_mul_hi_u32 s7, s5, s77
	s_add_i32 s78, s58, 3
	s_add_i32 s7, s7, s6
	s_mul_i32 s6, s5, s77
	s_min_i32 s5, s78, s4
	v_lshl_add_u64 v[6:7], s[6:7], 2, v[0:1]
	s_ashr_i32 s6, s5, 31
	s_mul_i32 s6, s6, s77
	s_mul_hi_u32 s7, s5, s77
	s_add_i32 s79, s58, 4
	s_add_i32 s7, s7, s6
	s_mul_i32 s6, s5, s77
	s_min_i32 s5, s79, s4
	v_lshl_add_u64 v[16:17], s[6:7], 2, v[0:1]
	s_ashr_i32 s6, s5, 31
	s_mul_i32 s6, s6, s77
	s_mul_hi_u32 s7, s5, s77
	s_add_i32 s80, s58, 5
	s_add_i32 s7, s7, s6
	s_mul_i32 s6, s5, s77
	s_min_i32 s5, s80, s4
	v_lshl_add_u64 v[22:23], s[6:7], 2, v[0:1]
	s_ashr_i32 s6, s5, 31
	s_mul_i32 s6, s6, s77
	s_mul_hi_u32 s7, s5, s77
	s_add_i32 s81, s58, 6
	s_add_i32 s7, s7, s6
	s_mul_i32 s6, s5, s77
	s_min_i32 s5, s81, s4
	v_lshl_add_u64 v[24:25], s[6:7], 2, v[0:1]
	s_ashr_i32 s6, s5, 31
	s_mul_i32 s6, s6, s77
	s_mul_hi_u32 s7, s5, s77
	s_add_i32 s82, s58, 7
	s_add_i32 s7, s7, s6
	s_mul_i32 s6, s5, s77
	s_min_i32 s5, s82, s4
	v_lshl_add_u64 v[26:27], s[6:7], 2, v[0:1]
	s_ashr_i32 s6, s5, 31
	s_mul_i32 s6, s6, s77
	s_mul_hi_u32 s7, s5, s77
	s_add_i32 s83, s58, 8
	s_add_i32 s7, s7, s6
	s_mul_i32 s6, s5, s77
	s_min_i32 s5, s83, s4
	v_lshl_add_u64 v[28:29], s[6:7], 2, v[0:1]
	s_ashr_i32 s6, s5, 31
	s_mul_i32 s6, s6, s77
	s_mul_hi_u32 s7, s5, s77
	s_add_i32 s85, s58, 9
	s_add_i32 s7, s7, s6
	s_mul_i32 s6, s5, s77
	s_min_i32 s5, s85, s4
	global_load_dword v21, v[2:3], off
	global_load_dword v20, v[4:5], off
	global_load_dword v19, v[6:7], off
	global_load_dword v18, v[16:17], off
	s_nop 0
	global_load_dword v17, v[22:23], off
	global_load_dword v16, v[24:25], off
	global_load_dword v15, v[26:27], off
	global_load_dword v8, v[28:29], off
	v_lshl_add_u64 v[2:3], s[6:7], 2, v[0:1]
	s_ashr_i32 s6, s5, 31
	s_mul_i32 s6, s6, s77
	s_mul_hi_u32 s7, s5, s77
	s_add_i32 s86, s58, 10
	s_add_i32 s7, s7, s6
	s_mul_i32 s6, s5, s77
	s_min_i32 s5, s86, s4
	v_lshl_add_u64 v[4:5], s[6:7], 2, v[0:1]
	s_ashr_i32 s6, s5, 31
	s_mul_i32 s6, s6, s77
	s_mul_hi_u32 s7, s5, s77
	s_add_i32 s87, s58, 11
	s_add_i32 s7, s7, s6
	s_mul_i32 s6, s5, s77
	s_min_i32 s5, s87, s4
	v_lshl_add_u64 v[6:7], s[6:7], 2, v[0:1]
	s_ashr_i32 s6, s5, 31
	s_mul_i32 s6, s6, s77
	s_mul_hi_u32 s7, s5, s77
	s_add_i32 s88, s58, 12
	s_add_i32 s7, s7, s6
	s_mul_i32 s6, s5, s77
	s_min_i32 s5, s88, s4
	v_lshl_add_u64 v[22:23], s[6:7], 2, v[0:1]
	s_ashr_i32 s6, s5, 31
	s_mul_i32 s6, s6, s77
	s_mul_hi_u32 s7, s5, s77
	s_add_i32 s89, s58, 13
	s_add_i32 s7, s7, s6
	s_mul_i32 s6, s5, s77
	s_min_i32 s5, s89, s4
	v_lshl_add_u64 v[24:25], s[6:7], 2, v[0:1]
	s_ashr_i32 s6, s5, 31
	s_mul_i32 s6, s6, s77
	s_mul_hi_u32 s7, s5, s77
	s_add_i32 s90, s58, 14
	s_add_i32 s7, s7, s6
	s_mul_i32 s6, s5, s77
	s_min_i32 s5, s90, s4
	v_lshl_add_u64 v[30:31], s[6:7], 2, v[0:1]
	s_ashr_i32 s6, s5, 31
	s_mul_i32 s6, s6, s77
	s_mul_hi_u32 s7, s5, s77
	s_add_i32 s92, s58, 15
	s_add_i32 s7, s7, s6
	s_mul_i32 s6, s5, s77
	s_min_i32 s5, s92, s4
	v_lshl_add_u64 v[32:33], s[6:7], 2, v[0:1]
	s_ashr_i32 s6, s5, 31
	s_mul_i32 s6, s6, s77
	s_mul_hi_u32 s7, s5, s77
	s_add_i32 s93, s58, 16
	s_add_i32 s7, s7, s6
	s_mul_i32 s6, s5, s77
	s_min_i32 s5, s93, s4
	v_lshl_add_u64 v[34:35], s[6:7], 2, v[0:1]
	s_ashr_i32 s6, s5, 31
	s_mul_i32 s6, s6, s77
	s_mul_hi_u32 s7, s5, s77
	s_add_i32 s94, s58, 17
	s_add_i32 s7, s7, s6
	s_mul_i32 s6, s5, s77
	s_min_i32 s5, s94, s4
	global_load_dword v29, v[2:3], off
	global_load_dword v28, v[4:5], off
	global_load_dword v27, v[6:7], off
	global_load_dword v26, v[22:23], off
	s_nop 0
	global_load_dword v25, v[24:25], off
	s_nop 0
	global_load_dword v24, v[30:31], off
	global_load_dword v23, v[32:33], off
	global_load_dword v22, v[34:35], off
	v_lshl_add_u64 v[2:3], s[6:7], 2, v[0:1]
	s_ashr_i32 s6, s5, 31
	s_mul_i32 s6, s6, s77
	s_mul_hi_u32 s7, s5, s77
	s_add_i32 s95, s58, 18
	s_add_i32 s7, s7, s6
	s_mul_i32 s6, s5, s77
	s_min_i32 s5, s95, s4
	v_lshl_add_u64 v[4:5], s[6:7], 2, v[0:1]
	s_ashr_i32 s6, s5, 31
	s_mul_i32 s6, s6, s77
	s_mul_hi_u32 s7, s5, s77
	s_add_i32 s50, s58, 19
	s_add_i32 s7, s7, s6
	s_mul_i32 s6, s5, s77
	s_min_i32 s5, s50, s4
	v_lshl_add_u64 v[6:7], s[6:7], 2, v[0:1]
	s_ashr_i32 s6, s5, 31
	s_mul_i32 s6, s6, s77
	s_mul_hi_u32 s7, s5, s77
	s_add_i32 s51, s58, 20
	s_add_i32 s7, s7, s6
	s_mul_i32 s6, s5, s77
	s_min_i32 s5, s51, s4
	v_lshl_add_u64 v[30:31], s[6:7], 2, v[0:1]
	s_ashr_i32 s6, s5, 31
	s_mul_i32 s6, s6, s77
	s_mul_hi_u32 s7, s5, s77
	s_add_i32 s52, s58, 21
	s_add_i32 s7, s7, s6
	s_mul_i32 s6, s5, s77
	s_min_i32 s5, s52, s4
	v_lshl_add_u64 v[32:33], s[6:7], 2, v[0:1]
	s_ashr_i32 s6, s5, 31
	s_mul_i32 s6, s6, s77
	s_mul_hi_u32 s7, s5, s77
	s_add_i32 s53, s58, 22
	s_add_i32 s7, s7, s6
	s_mul_i32 s6, s5, s77
	s_min_i32 s5, s53, s4
	v_lshl_add_u64 v[38:39], s[6:7], 2, v[0:1]
	s_ashr_i32 s6, s5, 31
	s_mul_i32 s6, s6, s77
	s_mul_hi_u32 s7, s5, s77
	s_add_i32 s7, s7, s6
	s_mul_i32 s6, s5, s77
; __device__ __forceinline__ void conv_load(const ConvItem& ci, int lane, float (&v)[64]) {
;     ...
; #pragma unroll
;     for (int i = 0; i < 64; ++i) { const int k = ci.k0 + i, kk = k < kmax ? k : kmax; v[i] = __builtin_nontemporal_load(base + (size_t)kk * ci.ldw); }
	v_lshl_add_u64 v[40:41], s[6:7], 2, v[0:1]
	s_add_i32 s6, s58, 23
	s_min_i32 s5, s6, s4
	s_ashr_i32 s7, s5, 31
	s_mul_i32 s7, s7, s77
	s_mul_hi_u32 s8, s5, s77
	s_add_i32 s9, s8, s7
	s_add_i32 s7, s58, 24
	s_mul_i32 s8, s5, s77
	s_min_i32 s5, s7, s4
	v_lshl_add_u64 v[42:43], s[8:9], 2, v[0:1]
	s_ashr_i32 s8, s5, 31
	s_mul_i32 s8, s8, s77
	s_mul_hi_u32 s9, s5, s77
	s_add_i32 s9, s9, s8
	s_mul_i32 s8, s5, s77
	global_load_dword v37, v[2:3], off
	global_load_dword v36, v[4:5], off
	global_load_dword v35, v[6:7], off
	global_load_dword v34, v[30:31], off
	s_nop 0
	global_load_dword v33, v[32:33], off
	s_nop 0
	global_load_dword v32, v[38:39], off
	global_load_dword v31, v[40:41], off
	global_load_dword v30, v[42:43], off
	v_lshl_add_u64 v[2:3], s[8:9], 2, v[0:1]
	s_add_i32 s8, s58, 25
	s_min_i32 s5, s8, s4
	s_ashr_i32 s9, s5, 31
	s_mul_i32 s9, s9, s77
	s_mul_hi_u32 s10, s5, s77
	s_add_i32 s11, s10, s9
	s_add_i32 s9, s58, 26
	s_mul_i32 s10, s5, s77
	s_min_i32 s5, s9, s4
	v_lshl_add_u64 v[4:5], s[10:11], 2, v[0:1]
	s_ashr_i32 s10, s5, 31
	s_mul_i32 s10, s10, s77
	s_mul_hi_u32 s11, s5, s77
	s_add_i32 s11, s11, s10
	s_mul_i32 s10, s5, s77
	v_lshl_add_u64 v[6:7], s[10:11], 2, v[0:1]
	s_add_i32 s10, s58, 27
	s_min_i32 s5, s10, s4
	s_ashr_i32 s11, s5, 31
	s_mul_i32 s11, s11, s77
	s_mul_hi_u32 s12, s5, s77
	s_add_i32 s13, s12, s11
	s_add_i32 s11, s58, 28
	s_mul_i32 s12, s5, s77
	s_min_i32 s5, s11, s4
	v_lshl_add_u64 v[38:39], s[12:13], 2, v[0:1]
	s_ashr_i32 s12, s5, 31
	s_mul_i32 s12, s12, s77
	s_mul_hi_u32 s13, s5, s77
	s_add_i32 s14, s58, 29
	s_add_i32 s13, s13, s12
	s_mul_i32 s12, s5, s77
	s_min_i32 s5, s14, s4
	v_lshl_add_u64 v[40:41], s[12:13], 2, v[0:1]
	s_ashr_i32 s12, s5, 31
	s_mul_i32 s12, s12, s77
	s_mul_hi_u32 s13, s5, s77
	s_add_i32 s15, s58, 30
	s_add_i32 s13, s13, s12
	s_mul_i32 s12, s5, s77
	s_min_i32 s5, s15, s4
	v_lshl_add_u64 v[46:47], s[12:13], 2, v[0:1]
	s_ashr_i32 s12, s5, 31
	s_mul_i32 s12, s12, s77
	s_mul_hi_u32 s13, s5, s77
	s_add_i32 s16, s58, 31
	s_add_i32 s13, s13, s12
	s_mul_i32 s12, s5, s77
	s_min_i32 s5, s16, s4
	v_lshl_add_u64 v[48:49], s[12:13], 2, v[0:1]
	s_ashr_i32 s12, s5, 31
	s_mul_i32 s12, s12, s77
	s_mul_hi_u32 s13, s5, s77
	s_add_i32 s17, s58, 32
	s_add_i32 s13, s13, s12
	s_mul_i32 s12, s5, s77
	s_min_i32 s5, s17, s4
	v_lshl_add_u64 v[50:51], s[12:13], 2, v[0:1]
	s_ashr_i32 s12, s5, 31
	s_mul_i32 s12, s12, s77
	s_mul_hi_u32 s13, s5, s77
	s_add_i32 s13, s13, s12
	s_mul_i32 s12, s5, s77
	global_load_dword v45, v[2:3], off
	global_load_dword v44, v[4:5], off
	global_load_dword v43, v[6:7], off
	global_load_dword v42, v[38:39], off
	s_nop 0
	global_load_dword v41, v[40:41], off
	s_nop 0
	global_load_dword v40, v[46:47], off
	global_load_dword v39, v[48:49], off
	global_load_dword v38, v[50:51], off
	v_lshl_add_u64 v[2:3], s[12:13], 2, v[0:1]
	s_add_i32 s12, s58, 33
	s_min_i32 s5, s12, s4
	s_ashr_i32 s13, s5, 31
	s_mul_i32 s13, s13, s77
	s_mul_hi_u32 s18, s5, s77
	s_add_i32 s19, s18, s13
	s_add_i32 s13, s58, 34
	s_mul_i32 s18, s5, s77
	s_min_i32 s5, s13, s4
	v_lshl_add_u64 v[4:5], s[18:19], 2, v[0:1]
	s_ashr_i32 s18, s5, 31
	s_mul_i32 s18, s18, s77
	s_mul_hi_u32 s19, s5, s77
	s_add_i32 s20, s58, 35
	s_add_i32 s19, s19, s18
	s_mul_i32 s18, s5, s77
	s_min_i32 s5, s20, s4
	v_lshl_add_u64 v[6:7], s[18:19], 2, v[0:1]
	s_ashr_i32 s18, s5, 31
	s_mul_i32 s18, s18, s77
	s_mul_hi_u32 s19, s5, s77
	s_add_i32 s21, s58, 36
	s_add_i32 s19, s19, s18
	s_mul_i32 s18, s5, s77
	s_min_i32 s5, s21, s4
	v_lshl_add_u64 v[46:47], s[18:19], 2, v[0:1]
	s_ashr_i32 s18, s5, 31
	s_mul_i32 s18, s18, s77
	s_mul_hi_u32 s19, s5, s77
	s_add_i32 s24, s58, 37
	s_add_i32 s19, s19, s18
	s_mul_i32 s18, s5, s77
	s_min_i32 s5, s24, s4
	v_lshl_add_u64 v[48:49], s[18:19], 2, v[0:1]
	s_ashr_i32 s18, s5, 31
	s_mul_i32 s18, s18, s77
	s_mul_hi_u32 s19, s5, s77
	s_add_i32 s25, s58, 38
	s_add_i32 s19, s19, s18
	s_mul_i32 s18, s5, s77
	s_min_i32 s5, s25, s4
	v_lshl_add_u64 v[54:55], s[18:19], 2, v[0:1]
	s_ashr_i32 s18, s5, 31
	s_mul_i32 s18, s18, s77
	s_mul_hi_u32 s19, s5, s77
	s_add_i32 s26, s58, 39
	s_add_i32 s19, s19, s18
	s_mul_i32 s18, s5, s77
	s_min_i32 s5, s26, s4
	v_lshl_add_u64 v[56:57], s[18:19], 2, v[0:1]
	s_ashr_i32 s18, s5, 31
	s_mul_i32 s18, s18, s77
	s_mul_hi_u32 s19, s5, s77
	s_add_i32 s27, s58, 40
	s_add_i32 s19, s19, s18
	s_mul_i32 s18, s5, s77
	s_min_i32 s5, s27, s4
	v_lshl_add_u64 v[58:59], s[18:19], 2, v[0:1]
	s_ashr_i32 s18, s5, 31
	s_mul_i32 s18, s18, s77
	s_mul_hi_u32 s19, s5, s77
	s_add_i32 s19, s19, s18
	s_mul_i32 s18, s5, s77
	global_load_dword v53, v[2:3], off
	global_load_dword v52, v[4:5], off
	global_load_dword v51, v[6:7], off
	global_load_dword v50, v[46:47], off
	s_nop 0
	global_load_dword v49, v[48:49], off
	s_nop 0
	global_load_dword v48, v[54:55], off
	global_load_dword v47, v[56:57], off
	global_load_dword v46, v[58:59], off
	v_lshl_add_u64 v[2:3], s[18:19], 2, v[0:1]
	s_add_i32 s18, s58, 41
	s_min_i32 s5, s18, s4
	s_ashr_i32 s19, s5, 31
	s_mul_i32 s19, s19, s77
	s_mul_hi_u32 s22, s5, s77
	s_add_i32 s23, s22, s19
	s_add_i32 s19, s58, 42
	s_mul_i32 s22, s5, s77
	s_min_i32 s5, s19, s4
	v_lshl_add_u64 v[4:5], s[22:23], 2, v[0:1]
	s_ashr_i32 s22, s5, 31
	s_mul_i32 s22, s22, s77
	s_mul_hi_u32 s23, s5, s77
	s_add_i32 s28, s58, 43
	s_add_i32 s23, s23, s22
	s_mul_i32 s22, s5, s77
	s_min_i32 s5, s28, s4
	v_lshl_add_u64 v[6:7], s[22:23], 2, v[0:1]
	s_ashr_i32 s22, s5, 31
	s_mul_i32 s22, s22, s77
	s_mul_hi_u32 s23, s5, s77
	s_add_i32 s29, s58, 44
	s_add_i32 s23, s23, s22
	s_mul_i32 s22, s5, s77
	s_min_i32 s5, s29, s4
; __device__ __forceinline__ void conv_load(const ConvItem& ci, int lane, float (&v)[64]) {
;     ...
; #pragma unroll
;     for (int i = 0; i < 64; ++i) { const int k = ci.k0 + i, kk = k < kmax ? k : kmax; v[i] = __builtin_nontemporal_load(base + (size_t)kk * ci.ldw); }
; __device__ __forceinline__ void conv_store(const ConvItem& ci, LAS float* scr, int lane, const float (&v)[64]) {
;     const int c = lane & 7;
;     f32x4 s0 = {1.f, 1.f, 1.f, 1.f}, s1 = s0;
;     if (ci.ks) { const int kb = ci.k0 + 8 * c < ci.Ksrc - 8 ? ci.k0 + 8 * c : ci.Ksrc - 8; s0 = *(const f32x4*)(ci.ks + kb); s1 = *(const f32x4*)(ci.ks + kb + 4); }
	v_lshl_add_u64 v[54:55], s[22:23], 2, v[0:1]
	s_ashr_i32 s22, s5, 31
	s_mul_i32 s22, s22, s77
	s_mul_hi_u32 s23, s5, s77
	s_add_i32 s23, s23, s22
	s_mul_i32 s22, s5, s77
	v_lshl_add_u64 v[56:57], s[22:23], 2, v[0:1]
	s_add_i32 s22, s58, 45
	s_min_i32 s5, s22, s4
	s_ashr_i32 s23, s5, 31
	s_mul_i32 s23, s23, s77
	s_mul_hi_u32 s30, s5, s77
	s_add_i32 s31, s30, s23
	s_add_i32 s23, s58, 46
	s_mul_i32 s30, s5, s77
	s_min_i32 s5, s23, s4
	v_lshl_add_u64 v[62:63], s[30:31], 2, v[0:1]
	s_ashr_i32 s30, s5, 31
	s_mul_i32 s30, s30, s77
	s_mul_hi_u32 s31, s5, s77
	s_add_i32 s31, s31, s30
	s_mul_i32 s30, s5, s77
	v_lshl_add_u64 v[64:65], s[30:31], 2, v[0:1]
	s_add_i32 s30, s58, 47
	s_min_i32 s5, s30, s4
	s_ashr_i32 s31, s5, 31
	s_mul_i32 s31, s31, s77
	s_mul_hi_u32 s34, s5, s77
	s_add_i32 s35, s34, s31
	s_add_i32 s31, s58, 48
	s_mul_i32 s34, s5, s77
	s_min_i32 s5, s31, s4
	v_lshl_add_u64 v[66:67], s[34:35], 2, v[0:1]
	s_ashr_i32 s34, s5, 31
	s_mul_i32 s34, s34, s77
	s_mul_hi_u32 s35, s5, s77
	s_add_i32 s36, s58, 49
	s_add_i32 s35, s35, s34
	s_mul_i32 s34, s5, s77
	s_min_i32 s5, s36, s4
	global_load_dword v61, v[2:3], off
	global_load_dword v60, v[4:5], off
	global_load_dword v59, v[6:7], off
	global_load_dword v58, v[54:55], off
	s_nop 0
	global_load_dword v57, v[56:57], off
	s_nop 0
	global_load_dword v56, v[62:63], off
	global_load_dword v55, v[64:65], off
	global_load_dword v54, v[66:67], off
	v_lshl_add_u64 v[2:3], s[34:35], 2, v[0:1]
	s_ashr_i32 s34, s5, 31
	s_mul_i32 s34, s34, s77
	s_mul_hi_u32 s35, s5, s77
	s_add_i32 s37, s58, 50
	s_add_i32 s35, s35, s34
	s_mul_i32 s34, s5, s77
	s_min_i32 s5, s37, s4
	v_lshl_add_u64 v[4:5], s[34:35], 2, v[0:1]
	s_ashr_i32 s34, s5, 31
	s_mul_i32 s34, s34, s77
	s_mul_hi_u32 s35, s5, s77
	s_add_i32 s38, s58, 51
	s_add_i32 s35, s35, s34
	s_mul_i32 s34, s5, s77
	s_min_i32 s5, s38, s4
	v_lshl_add_u64 v[6:7], s[34:35], 2, v[0:1]
	s_ashr_i32 s34, s5, 31
	s_mul_i32 s34, s34, s77
	s_mul_hi_u32 s35, s5, s77
	s_add_i32 s39, s58, 52
	s_add_i32 s35, s35, s34
	s_mul_i32 s34, s5, s77
	s_min_i32 s5, s39, s4
	v_lshl_add_u64 v[62:63], s[34:35], 2, v[0:1]
	s_ashr_i32 s34, s5, 31
	s_mul_i32 s34, s34, s77
	s_mul_hi_u32 s35, s5, s77
	s_add_i32 s35, s35, s34
	s_mul_i32 s34, s5, s77
	v_lshl_add_u64 v[64:65], s[34:35], 2, v[0:1]
	s_add_i32 s34, s58, 53
	s_min_i32 s5, s34, s4
	s_ashr_i32 s35, s5, 31
	s_mul_i32 s35, s35, s77
	s_mul_hi_u32 s42, s5, s77
	s_add_i32 s43, s42, s35
	s_add_i32 s35, s58, 54
	s_mul_i32 s42, s5, s77
	s_min_i32 s5, s35, s4
	v_lshl_add_u64 v[72:73], s[42:43], 2, v[0:1]
	s_ashr_i32 s42, s5, 31
	s_mul_i32 s42, s42, s77
	s_mul_hi_u32 s43, s5, s77
	s_add_i32 s43, s43, s42
	s_mul_i32 s42, s5, s77
	v_lshl_add_u64 v[74:75], s[42:43], 2, v[0:1]
	s_add_i32 s42, s58, 55
	s_min_i32 s5, s42, s4
	s_ashr_i32 s43, s5, 31
	s_mul_i32 s43, s43, s77
	s_mul_hi_u32 s44, s5, s77
	s_add_i32 s45, s44, s43
	s_add_i32 s43, s58, 56
	s_mul_i32 s44, s5, s77
	s_min_i32 s5, s43, s4
	v_lshl_add_u64 v[76:77], s[44:45], 2, v[0:1]
	s_ashr_i32 s44, s5, 31
	s_mul_i32 s44, s44, s77
	s_mul_hi_u32 s45, s5, s77
	s_add_i32 s54, s58, 57
	s_add_i32 s45, s45, s44
	s_mul_i32 s44, s5, s77
	s_min_i32 s5, s54, s4
	global_load_dword v70, v[2:3], off
	global_load_dword v69, v[4:5], off
	global_load_dword v68, v[6:7], off
	global_load_dword v67, v[62:63], off
	global_load_dword v66, v[64:65], off
	s_nop 0
	global_load_dword v64, v[72:73], off
	global_load_dword v63, v[74:75], off
	global_load_dword v62, v[76:77], off
	v_lshl_add_u64 v[2:3], s[44:45], 2, v[0:1]
	s_ashr_i32 s44, s5, 31
	s_mul_i32 s44, s44, s77
	s_mul_hi_u32 s45, s5, s77
	s_add_i32 s55, s58, 58
	s_add_i32 s45, s45, s44
	s_mul_i32 s44, s5, s77
	s_min_i32 s5, s55, s4
	global_load_dword v65, v[2:3], off
	v_lshl_add_u64 v[2:3], s[44:45], 2, v[0:1]
	s_ashr_i32 s44, s5, 31
	s_mul_i32 s44, s44, s77
	s_mul_hi_u32 s45, s5, s77
	s_add_i32 s46, s58, 59
	s_add_i32 s45, s45, s44
	s_mul_i32 s44, s5, s77
	s_min_i32 s5, s46, s4
	v_lshl_add_u64 v[4:5], s[44:45], 2, v[0:1]
	s_ashr_i32 s44, s5, 31
	s_mul_i32 s44, s44, s77
	s_mul_hi_u32 s45, s5, s77
	s_add_i32 s47, s58, 60
	s_add_i32 s45, s45, s44
	s_mul_i32 s44, s5, s77
	s_min_i32 s5, s47, s4
	v_lshl_add_u64 v[6:7], s[44:45], 2, v[0:1]
	s_ashr_i32 s44, s5, 31
	s_mul_i32 s44, s44, s77
	s_mul_hi_u32 s45, s5, s77
	s_add_i32 s48, s58, 61
	s_add_i32 s45, s45, s44
	s_mul_i32 s44, s5, s77
	s_min_i32 s5, s48, s4
	v_lshl_add_u64 v[76:77], s[44:45], 2, v[0:1]
	s_ashr_i32 s44, s5, 31
	s_mul_i32 s44, s44, s77
	s_mul_hi_u32 s45, s5, s77
	s_add_i32 s49, s58, 62
	s_add_i32 s45, s45, s44
	s_mul_i32 s44, s5, s77
	s_min_i32 s5, s49, s4
	global_load_dword v74, v[2:3], off
	global_load_dword v73, v[4:5], off
	global_load_dword v72, v[6:7], off
	global_load_dword v71, v[76:77], off
	v_lshl_add_u64 v[2:3], s[44:45], 2, v[0:1]
	s_ashr_i32 s44, s5, 31
	s_mul_i32 s44, s44, s77
	s_mul_hi_u32 s45, s5, s77
	s_add_i32 s45, s45, s44
	s_mul_i32 s44, s5, s77
	v_lshl_add_u64 v[4:5], s[44:45], 2, v[0:1]
	s_add_i32 s44, s58, 63
	s_min_i32 s4, s44, s4
	s_ashr_i32 s5, s4, 31
	s_mul_i32 s5, s5, s77
	s_mul_hi_u32 s45, s4, s77
	s_add_i32 s5, s45, s5
	s_mul_i32 s4, s4, s77
	v_lshl_add_u64 v[0:1], s[4:5], 2, v[0:1]
	global_load_dword v77, v[2:3], off
	global_load_dword v76, v[4:5], off
	global_load_dword v75, v[0:1], off
	s_cmp_eq_u64 s[62:63], 0
	s_cbranch_scc0 .Lcvp10_29
	v_mov_b32_e32 v0, 1.0
	v_mov_b32_e32 v1, 1.0
	v_mov_b32_e32 v2, 1.0
	v_mov_b32_e32 v3, 1.0
	v_mov_b32_e32 v4, 1.0
	v_mov_b32_e32 v5, 1.0
	v_mov_b32_e32 v6, 1.0
	v_mov_b32_e32 v7, 1.0
	s_branch .Lcvp10_30
